# K3 count phase straight-line with address reuse in msplit
# baseline (speedup 1.0000x reference)
.LBB2_17:
	s_or_b64 exec, exec, s[38:39]
	s_mov_b64 s[2:3], exec
	v_mov_b32_e32 v100, 1
	s_waitcnt vmcnt(15)
	v_cndmask_b32_e64 v19, -1, v18, s[20:21]
	v_mul_u32_u24_e32 v18, 0x640, v6
	v_or_b32_e32 v18, 0x10000, v18
	s_and_b64 exec, s[2:3], s[20:21]
	v_lshrrev_b32_e32 v84, 15, v19
	v_and_b32_e32 v84, 0x1fffc, v84
	v_add_u32_e32 v84, v18, v84
	ds_add_u32 v84, v100
	s_mov_b64 exec, s[2:3]
	s_waitcnt vmcnt(14)
	v_cndmask_b32_e64 v20, -1, v16, s[8:9]
	s_and_b64 exec, s[2:3], s[8:9]
	v_lshrrev_b32_e32 v85, 15, v20
	v_and_b32_e32 v85, 0x1fffc, v85
	v_add_u32_e32 v85, v18, v85
	ds_add_u32 v85, v100
	s_mov_b64 exec, s[2:3]
	s_waitcnt vmcnt(13)
	v_cndmask_b32_e64 v21, -1, v14, s[10:11]
	s_and_b64 exec, s[2:3], s[10:11]
	v_lshrrev_b32_e32 v86, 15, v21
	v_and_b32_e32 v86, 0x1fffc, v86
	v_add_u32_e32 v86, v18, v86
	ds_add_u32 v86, v100
	s_mov_b64 exec, s[2:3]
	s_waitcnt vmcnt(12)
	v_cndmask_b32_e64 v22, -1, v13, s[12:13]
	s_and_b64 exec, s[2:3], s[12:13]
	v_lshrrev_b32_e32 v87, 15, v22
	v_and_b32_e32 v87, 0x1fffc, v87
	v_add_u32_e32 v87, v18, v87
	ds_add_u32 v87, v100
	s_mov_b64 exec, s[2:3]
	s_waitcnt vmcnt(11)
	v_cndmask_b32_e64 v23, -1, v11, s[14:15]
	s_and_b64 exec, s[2:3], s[14:15]
	v_lshrrev_b32_e32 v88, 15, v23
	v_and_b32_e32 v88, 0x1fffc, v88
	v_add_u32_e32 v88, v18, v88
	ds_add_u32 v88, v100
	s_mov_b64 exec, s[2:3]
	s_waitcnt vmcnt(10)
	v_cndmask_b32_e64 v24, -1, v9, s[16:17]
	s_and_b64 exec, s[2:3], s[16:17]
	v_lshrrev_b32_e32 v89, 15, v24
	v_and_b32_e32 v89, 0x1fffc, v89
	v_add_u32_e32 v89, v18, v89
	ds_add_u32 v89, v100
	s_mov_b64 exec, s[2:3]
	s_waitcnt vmcnt(9)
	v_cndmask_b32_e64 v25, -1, v8, s[18:19]
	s_and_b64 exec, s[2:3], s[18:19]
	v_lshrrev_b32_e32 v90, 15, v25
	v_and_b32_e32 v90, 0x1fffc, v90
	v_add_u32_e32 v90, v18, v90
	ds_add_u32 v90, v100
	s_mov_b64 exec, s[2:3]
	s_waitcnt vmcnt(8)
	v_cndmask_b32_e64 v26, -1, v7, s[22:23]
	s_and_b64 exec, s[2:3], s[22:23]
	v_lshrrev_b32_e32 v91, 15, v26
	v_and_b32_e32 v91, 0x1fffc, v91
	v_add_u32_e32 v91, v18, v91
	ds_add_u32 v91, v100
	s_mov_b64 exec, s[2:3]
	s_waitcnt vmcnt(7)
	v_cndmask_b32_e64 v27, -1, v17, s[24:25]
	s_and_b64 exec, s[2:3], s[24:25]
	v_lshrrev_b32_e32 v92, 15, v27
	v_and_b32_e32 v92, 0x1fffc, v92
	v_add_u32_e32 v92, v18, v92
	ds_add_u32 v92, v100
	s_mov_b64 exec, s[2:3]
	s_waitcnt vmcnt(6)
	v_cndmask_b32_e64 v28, -1, v15, s[26:27]
	s_and_b64 exec, s[2:3], s[26:27]
	v_lshrrev_b32_e32 v93, 15, v28
	v_and_b32_e32 v93, 0x1fffc, v93
	v_add_u32_e32 v93, v18, v93
	ds_add_u32 v93, v100
	s_mov_b64 exec, s[2:3]
	s_waitcnt vmcnt(5)
	v_cndmask_b32_e64 v29, -1, v12, s[28:29]
	s_and_b64 exec, s[2:3], s[28:29]
	v_lshrrev_b32_e32 v94, 15, v29
	v_and_b32_e32 v94, 0x1fffc, v94
	v_add_u32_e32 v94, v18, v94
	ds_add_u32 v94, v100
	s_mov_b64 exec, s[2:3]
	s_waitcnt vmcnt(4)
	v_cndmask_b32_e64 v30, -1, v10, s[30:31]
	s_and_b64 exec, s[2:3], s[30:31]
	v_lshrrev_b32_e32 v95, 15, v30
	v_and_b32_e32 v95, 0x1fffc, v95
	v_add_u32_e32 v95, v18, v95
	ds_add_u32 v95, v100
	s_mov_b64 exec, s[2:3]
	s_waitcnt vmcnt(3)
	v_cndmask_b32_e64 v31, -1, v5, s[34:35]
	s_and_b64 exec, s[2:3], s[34:35]
	v_lshrrev_b32_e32 v96, 15, v31
	v_and_b32_e32 v96, 0x1fffc, v96
	v_add_u32_e32 v96, v18, v96
	ds_add_u32 v96, v100
	s_mov_b64 exec, s[2:3]
	s_waitcnt vmcnt(2)
	v_cndmask_b32_e64 v32, -1, v4, s[36:37]
	s_and_b64 exec, s[2:3], s[36:37]
	v_lshrrev_b32_e32 v97, 15, v32
	v_and_b32_e32 v97, 0x1fffc, v97
	v_add_u32_e32 v97, v18, v97
	ds_add_u32 v97, v100
	s_mov_b64 exec, s[2:3]
	s_waitcnt vmcnt(1)
	v_cndmask_b32_e64 v33, -1, v3, s[6:7]
	s_mov_b64 s[38:39], s[6:7]
	s_and_b64 exec, s[2:3], s[38:39]
	v_lshrrev_b32_e32 v98, 15, v33
	v_and_b32_e32 v98, 0x1fffc, v98
	v_add_u32_e32 v98, v18, v98
	ds_add_u32 v98, v100
	s_mov_b64 exec, s[2:3]
	s_waitcnt vmcnt(0)
	v_cndmask_b32_e32 v34, -1, v2, vcc
	s_mov_b64 s[40:41], vcc
	s_and_b64 exec, s[2:3], s[40:41]
	v_lshrrev_b32_e32 v99, 15, v34
	v_and_b32_e32 v99, 0x1fffc, v99
	v_add_u32_e32 v99, v18, v99
	ds_add_u32 v99, v100
	s_mov_b64 exec, s[2:3]
	s_max_u32 s88, s42, s50
	s_max_u32 s88, s88, s48
	s_max_u32 s88, s88, s43
	s_max_u32 s88, s88, s51
	s_max_u32 s88, s88, s49
	s_max_u32 s88, s88, s66
	s_max_u32 s88, s88, s65
	s_max_u32 s88, s88, s68
	s_max_u32 s88, s88, s67
	s_max_u32 s88, s88, s70
	s_max_u32 s88, s88, s69
	s_max_u32 s88, s88, s72
	s_max_u32 s88, s88, s71
	s_max_u32 s88, s88, s74
	s_max_u32 s88, s88, s73
	s_cmp_gt_u32 s88, 64
	s_cselect_b64 s[42:43], -1, 0
	v_cmp_lt_u32_e64 s[42:43], 64, v3
	s_and_b64 vcc, exec, s[42:43]
	s_cbranch_vccz .LBB2_99
	v_lshlrev_b32_e32 v2, 2, v48
	v_add_u32_e32 v7, 0x17450, v2
	ds_read_b32 v8, v7
	v_or_b32_e32 v4, 64, v45
	v_add_u32_e32 v5, 0x17850, v2
	s_waitcnt lgkmcnt(0)
	v_cmp_lt_u32_e32 vcc, v4, v8
	s_and_saveexec_b64 s[2:3], vcc
	s_cbranch_execz .LBB2_53
	ds_read_b32 v9, v5
	s_mov_b64 s[6:7], 0
	v_mov_b32_e32 v3, 0
	v_mov_b32_e32 v10, 1
	v_mov_b32_e32 v11, v4

.LBB2_135:
	s_or_b64 exec, exec, s[2:3]
	s_waitcnt lgkmcnt(3)
	v_add_u32_e32 v14, v15, v14
	v_add_u32_e32 v14, v14, v16
	v_add_u32_e32 v14, v14, v17
	s_waitcnt lgkmcnt(2)
	v_add_u32_e32 v6, v14, v6
	v_add_u32_e32 v6, v6, v7
	v_add_u32_e32 v6, v6, v8
	v_add_u32_e32 v6, v6, v9
	s_waitcnt lgkmcnt(1)
	v_add_u32_e32 v6, v6, v10
	v_add_u32_e32 v6, v6, v11
	v_add_u32_e32 v6, v6, v12
	v_add_u32_e32 v6, v6, v13
	s_waitcnt lgkmcnt(0)
	v_add_u32_e32 v2, v6, v2
	v_add_u32_e32 v2, v2, v3
	v_add_u32_e32 v2, v2, v4
	v_add_u32_e32 v2, v2, v5
	s_and_saveexec_b64 s[2:3], s[44:45]
	v_mov_b32_e32 v3, 0x17440
	ds_write_b32 v3, v2
	s_or_b64 exec, exec, s[2:3]
	s_movk_i32 s2, 0x4000
	v_cmp_lt_u32_e64 s[6:7], s2, v2
	s_movk_i32 s2, 0x4001
	v_cmp_gt_u32_e64 s[4:5], s2, v2
	s_mov_b64 s[2:3], -1
	s_and_b64 vcc, exec, s[4:5]
	s_waitcnt lgkmcnt(0)
	s_barrier
	s_cbranch_vccz .LBB2_252
	v_mov_b32_e32 v3, 1
	s_mov_b64 s[2:3], exec
	s_and_b64 exec, s[2:3], s[20:21]
	ds_add_rtn_u32 v66, v84, v3
	s_and_b64 exec, s[2:3], s[8:9]
	ds_add_rtn_u32 v67, v85, v3
	s_and_b64 exec, s[2:3], s[10:11]
	ds_add_rtn_u32 v68, v86, v3
	s_and_b64 exec, s[2:3], s[12:13]
	ds_add_rtn_u32 v69, v87, v3
	s_and_b64 exec, s[2:3], s[14:15]
	ds_add_rtn_u32 v70, v88, v3
	s_and_b64 exec, s[2:3], s[16:17]
	ds_add_rtn_u32 v71, v89, v3
	s_and_b64 exec, s[2:3], s[18:19]
	ds_add_rtn_u32 v72, v90, v3
	s_and_b64 exec, s[2:3], s[22:23]
	ds_add_rtn_u32 v73, v91, v3
	s_and_b64 exec, s[2:3], s[20:21]
	s_waitcnt lgkmcnt(7)
	v_lshlrev_b32_e32 v66, 2, v66
	ds_write_b32 v66, v19
	s_and_b64 exec, s[2:3], s[8:9]
	s_waitcnt lgkmcnt(7)
	v_lshlrev_b32_e32 v67, 2, v67
	ds_write_b32 v67, v20
	s_and_b64 exec, s[2:3], s[10:11]
	s_waitcnt lgkmcnt(7)
	v_lshlrev_b32_e32 v68, 2, v68
	ds_write_b32 v68, v21
	s_and_b64 exec, s[2:3], s[12:13]
	s_waitcnt lgkmcnt(7)
	v_lshlrev_b32_e32 v69, 2, v69
	ds_write_b32 v69, v22
	s_and_b64 exec, s[2:3], s[14:15]
	s_waitcnt lgkmcnt(7)
	v_lshlrev_b32_e32 v70, 2, v70
	ds_write_b32 v70, v23
	s_and_b64 exec, s[2:3], s[16:17]
	s_waitcnt lgkmcnt(7)
	v_lshlrev_b32_e32 v71, 2, v71
	ds_write_b32 v71, v24
	s_and_b64 exec, s[2:3], s[18:19]
	s_waitcnt lgkmcnt(7)
	v_lshlrev_b32_e32 v72, 2, v72
	ds_write_b32 v72, v25
	s_and_b64 exec, s[2:3], s[22:23]
	s_waitcnt lgkmcnt(7)
	v_lshlrev_b32_e32 v73, 2, v73
	ds_write_b32 v73, v26
	s_waitcnt lgkmcnt(6)
	s_and_b64 exec, s[2:3], s[24:25]
	ds_add_rtn_u32 v74, v92, v3
	s_and_b64 exec, s[2:3], s[26:27]
	ds_add_rtn_u32 v75, v93, v3
	s_and_b64 exec, s[2:3], s[28:29]
	ds_add_rtn_u32 v76, v94, v3
	s_and_b64 exec, s[2:3], s[30:31]
	ds_add_rtn_u32 v77, v95, v3
	s_and_b64 exec, s[2:3], s[34:35]
	ds_add_rtn_u32 v78, v96, v3
	s_and_b64 exec, s[2:3], s[36:37]
	ds_add_rtn_u32 v79, v97, v3
	s_and_b64 exec, s[2:3], s[38:39]
	ds_add_rtn_u32 v80, v98, v3
	s_and_b64 exec, s[2:3], s[40:41]
	ds_add_rtn_u32 v81, v99, v3
	s_and_b64 exec, s[2:3], s[24:25]
	s_waitcnt lgkmcnt(7)
	v_lshlrev_b32_e32 v74, 2, v74
	ds_write_b32 v74, v27
	s_and_b64 exec, s[2:3], s[26:27]
	s_waitcnt lgkmcnt(7)
	v_lshlrev_b32_e32 v75, 2, v75
	ds_write_b32 v75, v28
	s_and_b64 exec, s[2:3], s[28:29]
	s_waitcnt lgkmcnt(7)
	v_lshlrev_b32_e32 v76, 2, v76
	ds_write_b32 v76, v29
	s_and_b64 exec, s[2:3], s[30:31]
	s_waitcnt lgkmcnt(7)
	v_lshlrev_b32_e32 v77, 2, v77
	ds_write_b32 v77, v30
	s_and_b64 exec, s[2:3], s[34:35]
	s_waitcnt lgkmcnt(7)
	v_lshlrev_b32_e32 v78, 2, v78
	ds_write_b32 v78, v31
	s_and_b64 exec, s[2:3], s[36:37]
	s_waitcnt lgkmcnt(7)
	v_lshlrev_b32_e32 v79, 2, v79
	ds_write_b32 v79, v32
	s_and_b64 exec, s[2:3], s[38:39]
	s_waitcnt lgkmcnt(7)
	v_lshlrev_b32_e32 v80, 2, v80
	ds_write_b32 v80, v33
	s_and_b64 exec, s[2:3], s[40:41]
	s_waitcnt lgkmcnt(7)
	v_lshlrev_b32_e32 v81, 2, v81
	ds_write_b32 v81, v34
	s_mov_b64 exec, s[2:3]
	s_and_b64 vcc, exec, s[42:43]
	s_cbranch_vccz .LBB2_251
